# P0: conversion loop starts from the wave index rotated by a quarter grid (extra items land on workgroups without adaLN work)
# baseline (speedup 1.0000x reference)
.LBB0_50:
	s_cmpk_gt_i32 s97, 0x19bf
	s_cbranch_scc1 .LBB0_70
	v_lshrrev_b32_e32 v1, 5, v250
	s_movk_i32 s6, 0x84
	v_mov_b32_e32 v6, 0x630
	v_mad_u32_u24 v32, v1, s6, v6
	v_mov_b32_e32 v6, 0xc60
	v_mad_u32_u24 v39, v1, s6, v6
	v_mov_b32_e32 v6, 0x1290
	v_mad_u32_u24 v46, v1, s6, v6
	v_mov_b32_e32 v6, 0x18c0
	v_readlane_b32 s30, v254, 6
	v_mad_u32_u24 v53, v1, s6, v6
	v_lshlrev_b32_e32 v6, 3, v0
	s_lshl_b32 s3, s30, 14
	v_lshrrev_b32_e32 v61, 3, v250
	v_and_b32_e32 v6, 56, v6
	s_add_i32 s4, s3, 0
	v_mov_b32_e32 v3, 0
	v_mul_u32_u24_e32 v8, 0x84, v6
	v_lshlrev_b32_e32 v9, 2, v61
	v_lshlrev_b32_e32 v6, 1, v6
	v_mov_b32_e32 v7, v3
	v_add3_u32 v62, s4, v8, v9
	v_lshlrev_b32_e32 v8, 4, v0
	v_and_b32_e32 v20, 31, v0
	v_lshl_add_u64 v[10:11], s[72:73], 0, v[6:7]
	s_mov_b64 s[6:7], 0x3180000
	v_and_b32_e32 v14, 48, v8
	v_lshlrev_b32_e32 v2, 2, v20
	v_lshl_add_u64 v[6:7], v[10:11], 0, s[6:7]
	s_mov_b64 s[6:7], 0x2a00000
	v_mul_u32_u24_e32 v16, 0x84, v14
	v_mov_b32_e32 v15, v3
	v_and_b32_e32 v17, 60, v250
	s_add_u32 s3, s72, 0x2f00000
	v_add_u32_e32 v24, s4, v2
	v_lshl_add_u64 v[10:11], v[10:11], 0, s[6:7]
	v_lshl_add_u64 v[18:19], s[72:73], 0, v[14:15]
	s_mov_b64 s[6:7], 0x2480000
	v_add3_u32 v69, s4, v16, v17
	v_readlane_b32 s4, v254, 5
	s_addc_u32 s8, s73, 0
	v_lshl_add_u64 v[14:15], v[18:19], 0, s[6:7]
	s_mov_b64 s[6:7], 0x1980000
	s_bfe_u32 s4, s4, 0x20006
	v_lshl_add_u64 v[18:19], v[18:19], 0, s[6:7]
	s_lshl_b32 s6, s4, 5
	s_lshl_b32 s9, s4, 10
	s_lshl_b32 s4, s2, 8
	s_lshl_b32 s7, s30, 5
	v_readlane_b32 s31, v254, 7
	v_lshrrev_b32_e32 v68, 2, v250
	s_add_i32 s10, s4, s7
	s_lshl_b32 s4, s2, 4
	s_lshl_b32 s7, s30, 1
	s_mov_b32 s5, 0
	s_waitcnt lgkmcnt(0)
	v_lshl_add_u64 v[4:5], s[20:21], 0, v[2:3]
	v_mul_u32_u24_e32 v25, 0x84, v1
	v_or_b32_e32 v26, 2, v1
	v_or_b32_e32 v27, 4, v1
	v_or_b32_e32 v28, 6, v1
	v_or_b32_e32 v29, 8, v1
	v_or_b32_e32 v30, 10, v1
	v_or_b32_e32 v31, 12, v1
	v_or_b32_e32 v33, 14, v1
	v_or_b32_e32 v34, 16, v1
	v_or_b32_e32 v35, 18, v1
	v_or_b32_e32 v36, 20, v1
	v_or_b32_e32 v37, 22, v1
	v_or_b32_e32 v38, 24, v1
	v_or_b32_e32 v40, 26, v1
	v_or_b32_e32 v41, 28, v1
	v_or_b32_e32 v42, 30, v1
	v_or_b32_e32 v43, 32, v1
	v_or_b32_e32 v44, 34, v1
	v_or_b32_e32 v45, 36, v1
	v_or_b32_e32 v47, 38, v1
	v_or_b32_e32 v48, 40, v1
	v_or_b32_e32 v49, 42, v1
	v_or_b32_e32 v50, 44, v1
	v_or_b32_e32 v51, 46, v1
	v_or_b32_e32 v52, 48, v1
	v_or_b32_e32 v54, 50, v1
	v_or_b32_e32 v55, 52, v1
	v_or_b32_e32 v56, 54, v1
	v_or_b32_e32 v57, 56, v1
	v_or_b32_e32 v58, 58, v1
	v_or_b32_e32 v59, 60, v1
	v_or_b32_e32 v60, 62, v1
	v_or_b32_e32 v63, 8, v61
	v_or_b32_e32 v64, 16, v61
	v_or_b32_e32 v65, 24, v61
	v_and_b32_e32 v66, 0x70, v8
	v_bitop3_b32 v67, v61, 15, 24 bitop3:0xc8
	v_lshl_add_u64 v[8:9], s[60:61], 0, v[2:3]
	v_lshl_add_u64 v[12:13], s[58:59], 0, v[2:3]
	v_or_b32_e32 v70, 16, v68
	v_lshl_add_u64 v[16:17], s[56:57], 0, v[2:3]
	s_lshl_b32 s11, s28, 8
	s_add_i32 s20, s4, s7
	s_lshl_b32 s21, s28, 4
	s_lshl_b32 s29, s6, 2
	v_lshlrev_b32_e32 v20, 2, v20
	s_movk_i32 s30, 0x2000
	v_readlane_b32 s99, v254, 9
	s_nop 3
	s_lshr_b32 s98, s99, 2
	s_add_i32 s98, s97, s98
	s_sub_i32 s100, s98, s99
	s_cmp_ge_u32 s98, s99
	s_cselect_b32 s98, s100, s98
	s_lshl_b32 s10, s98, 5
	s_lshl_b32 s20, s98, 1
	s_mov_b32 s31, s98
	s_branch .LBB0_53
